# stack K1: J2 + two-batch row-scale load hoist in up-proj epilogue + out-proj epilogue residual loads requested earlier; key loops kept at the same 64-byte phase
# baseline (speedup 1.0000x reference)
.LBB0_2011:
	s_ashr_i32 s6, s11, 3
	s_lshl_b32 s60, s6, 8
	s_lshl_b32 s61, s6, 12
	s_lshl_b32 s6, s10, 8
	s_and_b32 s6, s6, 0xf00
	s_or_b32 s28, s61, s6
	s_add_i32 s8, s60, 0x4000
	s_and_b32 s12, s11, 7
	s_ashr_i32 s29, s28, 31
	s_mul_i32 s7, s28, 0xc00
	s_mul_hi_i32 s6, s28, 0xc00
	s_add_u32 s7, s35, s7
	s_addc_u32 s6, s36, s6
	s_mul_i32 s13, s12, 0x180
	s_add_u32 s10, s7, s13
	s_addc_u32 s11, s6, 0
	s_add_u32 s6, s37, s13
	s_addc_u32 s7, s38, 0
	s_lshl_b32 s59, s12, 7
	s_lshl_b32 s12, s12, 8
	s_add_u32 s30, s39, s12
	v_readfirstlane_b32 s62, v254
	s_addc_u32 s31, s40, 0
	s_ashr_i32 s12, s62, 6
	s_lshl_b32 s82, s12, 10
	s_mov_b32 s72, s6
	s_and_b32 s73, s7, 0xffff
	s_mov_b32 s74, 0x7ffffff0
	s_mov_b32 s75, 0x20000
	s_mov_b32 s76, s30
	s_and_b32 s77, s31, 0xffff
	s_mov_b32 s78, 0x7ffffff0
	s_mov_b32 s79, 0x20000
	v_lshl_add_u64 v[26:27], s[8:9], 0, v[142:143]
	v_lshl_add_u64 v[28:29], v[146:147], 0, s[8:9]
	v_lshl_or_b32 v2, s12, 5, v188
	v_mov_b64_e32 v[0:1], s[10:11]
	v_lshlrev_b64 v[16:17], 11, v[26:27]
	v_lshlrev_b64 v[18:19], 11, v[28:29]
	v_mad_i64_i32 v[0:1], s[10:11], v2, s44, v[0:1]
	v_lshl_add_u64 v[16:17], s[30:31], 0, v[16:17]
	v_lshl_add_u64 v[18:19], s[30:31], 0, v[18:19]
	v_lshl_add_u64 v[38:39], v[0:1], 0, v[148:149]
	v_lshl_add_u64 v[16:17], v[16:17], 0, v[150:151]
	v_lshl_add_u64 v[22:23], v[18:19], 0, v[150:151]
	global_load_dwordx4 v[0:3], v[38:39], off offset:256
	global_load_dwordx4 v[4:7], v[38:39], off offset:288
	global_load_dwordx4 v[8:11], v[38:39], off offset:320
	global_load_dwordx4 v[12:15], v[38:39], off offset:352
	global_load_dwordx4 v[18:21], v[16:17], off
	s_nop 0
	global_load_dwordx4 v[22:25], v[22:23], off
	v_mov_b64_e32 v[16:17], s[6:7]
	v_mad_u64_u32 v[30:31], s[10:11], v26, s44, v[16:17]
	v_mad_i32_i24 v31, v27, s44, v31
	v_lshl_add_u64 v[26:27], v[30:31], 0, v[150:151]
	v_mad_u64_u32 v[30:31], s[10:11], v28, s44, v[16:17]
	v_mad_i32_i24 v31, v29, s44, v31
	v_lshl_add_u64 v[30:31], v[30:31], 0, v[150:151]
	v_lshl_add_u64 v[34:35], s[8:9], 0, v[144:145]
	global_load_dwordx4 v[26:29], v[26:27], off
	s_nop 0
	global_load_dwordx4 v[30:33], v[30:31], off
	v_mad_u64_u32 v[36:37], s[10:11], v34, s44, v[16:17]
	v_mad_i32_i24 v37, v35, s44, v37
	v_lshl_add_u64 v[34:35], v[36:37], 0, v[152:153]
	global_load_dwordx4 v[34:37], v[34:35], off offset:256
	s_nop 0
	global_load_dwordx4 v[124:127], v[38:39], off
	global_load_dwordx4 v[120:123], v[38:39], off offset:32
	global_load_dwordx4 v[116:119], v[38:39], off offset:64
	global_load_dwordx4 v[112:115], v[38:39], off offset:96
	global_load_dwordx4 v[108:111], v[38:39], off offset:128
	global_load_dwordx4 v[104:107], v[38:39], off offset:160
	global_load_dwordx4 v[100:103], v[38:39], off offset:192
	global_load_dwordx4 v[96:99], v[38:39], off offset:224
	s_lshl_b32 s8, s12, 12
	v_add_u32_e32 v190, s8, v166
	v_add_u32_e32 v191, s45, v170
	v_add_u32_e32 v192, s45, v171
	v_add_u32_e32 v193, s45, v172
	v_add_u32_e32 v194, s45, v173
	s_mov_b32 s8, s9
	s_mov_b32 s10, s9
	s_mov_b32 s11, s9
	s_mov_b32 s12, s9
	s_mov_b32 s13, s9
	s_mov_b32 s14, s9
	s_mov_b32 s15, s9
	s_mov_b32 s16, s9
	s_mov_b32 s17, s9
	s_mov_b32 s18, s9
	s_mov_b32 s19, s9
	s_mov_b32 s20, s9
	s_mov_b32 s21, s9
	s_mov_b32 s22, s9
	s_mov_b32 s23, s9
	v_add_u32_e32 v195, 0, v168
	v_mov_b32_e32 v140, 0
	v_add_u32_e32 v196, 0x12000, v195
	v_lshrrev_b32_e32 v156, 4, v254
	v_and_b32_e32 v157, 15, v156
	v_and_b32_e32 v159, 15, v254
	v_xor_b32_e32 v157, v157, v159
	v_lshlrev_b32_e32 v157, 4, v157
	v_mad_u32_u24 v154, v156, s44, v157
	v_lshrrev_b32_e32 v156, 3, v254
	v_bfe_u32 v157, v254, 4, 3
	v_and_b32_e32 v159, 7, v254
	v_xor_b32_e32 v157, v157, v159
	v_lshlrev_b32_e32 v157, 4, v157
	v_add_u32_e32 v157, 0x100, v157
	v_mad_u32_u24 v155, v156, s44, v157
	v_and_b32_e32 v158, 3, v254
	v_lshlrev_b32_e32 v158, 4, v158
	v_bfe_u32 v156, v254, 5, 2
	v_lshl_or_b32 v158, v156, 6, v158
	v_bfe_u32 v156, v254, 2, 2
	v_lshl_or_b32 v158, v156, 11, v158
	v_bfe_u32 v156, v254, 7, 1
	v_lshl_or_b32 v158, v156, 13, v158
	v_bfe_u32 v156, v254, 4, 1
	v_lshl_or_b32 v158, v156, 14, v158
	v_bfe_u32 v156, v254, 8, 1
	v_lshl_or_b32 v158, v156, 15, v158
	s_waitcnt vmcnt(16)
	ds_write_b128 v190, v[0:3]
	s_waitcnt vmcnt(15)
	ds_write_b128 v190, v[4:7] offset:1024
	s_waitcnt vmcnt(14)
	ds_write_b128 v190, v[8:11] offset:2048
	s_waitcnt vmcnt(13)
	ds_write_b128 v190, v[12:15] offset:3072
	s_waitcnt vmcnt(0)
	s_waitcnt vmcnt(12)
	ds_write_b128 v175, v[18:21]
	s_waitcnt vmcnt(11)
	ds_write_b128 v176, v[22:25]
	s_waitcnt vmcnt(10)
	ds_write_b128 v177, v[26:29] offset:32768
	s_waitcnt vmcnt(9)
	ds_write_b128 v178, v[30:33] offset:32768
	s_waitcnt vmcnt(8)
	ds_write_b128 v179, v[34:37]
	s_waitcnt lgkmcnt(0)
	s_barrier
	ds_read_b128 v[0:3], v180 offset:32768
	ds_read_b128 v[4:7], v180 offset:40960
	s_waitcnt vmcnt(7) lgkmcnt(1)
	v_mfma_f32_32x32x16_bf16 v[48:63], v[0:3], v[124:127], 0
	s_waitcnt lgkmcnt(0)
	v_mfma_f32_32x32x16_bf16 v[64:79], v[4:7], v[124:127], 0
	ds_read_b128 v[0:3], v181 offset:32768
	ds_read_b128 v[4:7], v181 offset:40960
	s_waitcnt vmcnt(6) lgkmcnt(1)
	v_mfma_f32_32x32x16_bf16 v[48:63], v[0:3], v[120:123], v[48:63]
	s_waitcnt lgkmcnt(0)
	v_mfma_f32_32x32x16_bf16 v[64:79], v[4:7], v[120:123], v[64:79]
	ds_read_b128 v[0:3], v182 offset:32768
	ds_read_b128 v[4:7], v182 offset:40960
	s_waitcnt vmcnt(5) lgkmcnt(1)
	v_mfma_f32_32x32x16_bf16 v[48:63], v[0:3], v[116:119], v[48:63]
	s_waitcnt lgkmcnt(0)
	v_mfma_f32_32x32x16_bf16 v[64:79], v[4:7], v[116:119], v[64:79]
	ds_read_b128 v[0:3], v183 offset:32768
	ds_read_b128 v[4:7], v183 offset:40960
	s_waitcnt vmcnt(4) lgkmcnt(1)
	v_mfma_f32_32x32x16_bf16 v[48:63], v[0:3], v[112:115], v[48:63]
	s_waitcnt lgkmcnt(0)
	v_mfma_f32_32x32x16_bf16 v[64:79], v[4:7], v[112:115], v[64:79]
	ds_read_b128 v[0:3], v184 offset:32768
	ds_read_b128 v[4:7], v184 offset:40960
	s_waitcnt vmcnt(3) lgkmcnt(1)
	v_mfma_f32_32x32x16_bf16 v[48:63], v[0:3], v[108:111], v[48:63]
	s_waitcnt lgkmcnt(0)
	v_mfma_f32_32x32x16_bf16 v[64:79], v[4:7], v[108:111], v[64:79]
	ds_read_b128 v[0:3], v185 offset:32768
	ds_read_b128 v[4:7], v185 offset:40960
	s_waitcnt vmcnt(2) lgkmcnt(1)
	v_mfma_f32_32x32x16_bf16 v[48:63], v[0:3], v[104:107], v[48:63]
	s_waitcnt lgkmcnt(0)
	v_mfma_f32_32x32x16_bf16 v[64:79], v[4:7], v[104:107], v[64:79]
	ds_read_b128 v[0:3], v186 offset:32768
	ds_read_b128 v[4:7], v186 offset:40960
	s_waitcnt vmcnt(1) lgkmcnt(1)
	v_mfma_f32_32x32x16_bf16 v[48:63], v[0:3], v[100:103], v[48:63]
	s_waitcnt lgkmcnt(0)
	v_mfma_f32_32x32x16_bf16 v[64:79], v[4:7], v[100:103], v[64:79]
	ds_read_b128 v[0:3], v187 offset:32768
	ds_read_b128 v[4:7], v187 offset:40960
	s_waitcnt vmcnt(0) lgkmcnt(1)
	v_mfma_f32_32x32x16_bf16 v[48:63], v[0:3], v[96:99], v[48:63]
	s_waitcnt lgkmcnt(0)
	v_mfma_f32_32x32x16_bf16 v[64:79], v[4:7], v[96:99], v[64:79]
	ds_read_b128 v[0:3], v191
	ds_read_b128 v[4:7], v190
	ds_read_b128 v[8:11], v191 offset:4096
	ds_read_b128 v[12:15], v190 offset:1024
	s_waitcnt lgkmcnt(2)
	v_mfma_f32_32x32x16_bf16 v[48:63], v[0:3], v[4:7], v[48:63]
	s_waitcnt lgkmcnt(1)
	v_mfma_f32_32x32x16_bf16 v[64:79], v[8:11], v[4:7], v[64:79]
	ds_read_b128 v[0:3], v192
	ds_read_b128 v[4:7], v192 offset:4096
	s_waitcnt lgkmcnt(1)
	v_mfma_f32_32x32x16_bf16 v[48:63], v[0:3], v[12:15], v[48:63]
	s_waitcnt lgkmcnt(0)
	v_mfma_f32_32x32x16_bf16 v[64:79], v[4:7], v[12:15], v[64:79]
	ds_read_b128 v[0:3], v193
	ds_read_b128 v[4:7], v190 offset:2048
	ds_read_b128 v[8:11], v193 offset:4096
	ds_read_b128 v[18:21], v190 offset:3072
	ds_read_b128 v[22:25], v194 offset:4096
	s_waitcnt lgkmcnt(3)
	v_mfma_f32_32x32x16_bf16 v[48:63], v[0:3], v[4:7], v[48:63]
	ds_read_b128 v[0:3], v194
	s_waitcnt lgkmcnt(3)
	v_mfma_f32_32x32x16_bf16 v[64:79], v[8:11], v[4:7], v[64:79]
	s_waitcnt lgkmcnt(0)
	v_mfma_f32_32x32x16_bf16 v[48:63], v[0:3], v[18:21], v[48:63]
	v_mov_b64_e32 v[0:1], s[8:9]
	v_mov_b64_e32 v[2:3], s[10:11]
	v_mov_b64_e32 v[4:5], s[12:13]
	v_mov_b64_e32 v[6:7], s[14:15]
	v_mov_b64_e32 v[8:9], s[16:17]
	v_mov_b64_e32 v[10:11], s[18:19]
	v_mov_b64_e32 v[12:13], s[20:21]
	v_mfma_f32_32x32x16_bf16 v[64:79], v[22:25], v[18:21], v[64:79]
	s_nop 3
	v_max_f32_e32 v18, v49, v49
	v_max_f32_e32 v19, v48, v48
	v_max_f32_e32 v18, v19, v18
	v_max3_f32 v18, v18, v50, v51
	v_max3_f32 v18, v18, v52, v53
	v_max3_f32 v18, v18, v54, v55
	v_max3_f32 v18, v18, v56, v57
	v_max3_f32 v18, v18, v58, v59
	v_max3_f32 v18, v18, v60, v61
	v_max3_f32 v18, v18, v62, v63
	v_max3_f32 v18, v18, v64, v65
	v_max3_f32 v18, v18, v66, v67
	v_max3_f32 v18, v18, v68, v69
	v_max3_f32 v18, v18, v70, v71
	v_max3_f32 v18, v18, v72, v73
	v_max3_f32 v18, v18, v74, v75
	v_max3_f32 v18, v18, v76, v77
	v_max3_f32 v18, v18, v78, v79
	v_mov_b32_e32 v19, v18
	s_nop 1
	v_permlane32_swap_b32_e32 v18, v19
	v_mov_b64_e32 v[14:15], s[22:23]
	s_and_b32 s8, s62, 0x3fffffc0
	v_max_f32_e32 v19, v19, v19
	v_max_f32_e32 v18, v18, v18
	s_lshl_b32 s8, s8, 2
	v_max_f32_e32 v18, v18, v19
	s_add_i32 s12, s8, 0
	v_add_f32_e32 v19, 0x7149f2ca, v18
	s_add_i32 s12, s12, 0x14000
	v_cmp_ge_f32_e32 vcc, s46, v19
	s_cmp_eq_u64 vcc, exec
	s_cselect_b64 vcc, -1, 0
	s_add_i32 s8, s60, 0x4040
	v_max_f32_e32 v128, 0xf149f2ca, v18
	v_lshl_add_u64 v[18:19], s[8:9], 0, v[142:143]
	v_lshl_add_u64 v[20:21], v[146:147], 0, s[8:9]
	v_lshl_add_u64 v[22:23], s[8:9], 0, v[144:145]
	v_lshlrev_b64 v[24:25], 11, v[18:19]
	v_lshlrev_b64 v[26:27], 11, v[20:21]
	v_mad_u64_u32 v[28:29], s[10:11], v18, s44, v[16:17]
	v_mad_u64_u32 v[30:31], s[10:11], v20, s44, v[16:17]
	v_mad_u64_u32 v[16:17], s[10:11], v22, s44, v[16:17]
	v_lshl_add_u64 v[24:25], s[30:31], 0, v[24:25]
	v_lshl_add_u64 v[26:27], s[30:31], 0, v[26:27]
	v_mad_i32_i24 v29, v19, s44, v29
	v_mad_i32_i24 v31, v21, s44, v31
	v_mad_i32_i24 v17, v23, s44, v17
	v_lshl_add_u64 v[18:19], v[24:25], 0, v[150:151]
	v_lshl_add_u64 v[20:21], v[26:27], 0, v[150:151]
	v_lshl_add_u64 v[22:23], v[28:29], 0, v[150:151]
	v_lshl_add_u64 v[24:25], v[30:31], 0, v[150:151]
	v_lshl_add_u64 v[16:17], v[16:17], 0, v[152:153]
	global_load_dwordx4 v[80:83], v[18:19], off
	global_load_dwordx4 v[84:87], v[20:21], off
	global_load_dwordx4 v[88:91], v[22:23], off
	global_load_dwordx4 v[92:95], v[24:25], off
	global_load_dwordx4 v[200:203], v[16:17], off offset:256
	v_sub_f32_e32 v129, 0xf149f2ca, v128
	v_mul_f32_e32 v129, 0x3dd53b94, v129
	v_exp_f32_e32 v164, v129
	v_mov_b32_e32 v129, 0xf149f2ca
	v_cndmask_b32_e32 v198, v128, v129, vcc
	v_mul_f32_e32 v138, 0xbdd53b94, v198
	v_mov_b32_e32 v165, v138
	v_fmamk_f32 v48, v48, 0x3dd53b94, v138
	v_fmamk_f32 v49, v49, 0x3dd53b94, v138
	v_fmamk_f32 v50, v50, 0x3dd53b94, v138
	v_fmamk_f32 v51, v51, 0x3dd53b94, v138
	v_fmamk_f32 v52, v52, 0x3dd53b94, v138
	v_fmamk_f32 v53, v53, 0x3dd53b94, v138
	v_fmamk_f32 v54, v54, 0x3dd53b94, v138
	v_fmamk_f32 v55, v55, 0x3dd53b94, v138
	v_fmamk_f32 v56, v56, 0x3dd53b94, v138
	v_fmamk_f32 v57, v57, 0x3dd53b94, v138
	v_fmamk_f32 v58, v58, 0x3dd53b94, v138
	v_fmamk_f32 v59, v59, 0x3dd53b94, v138
	v_fmamk_f32 v60, v60, 0x3dd53b94, v138
	v_fmamk_f32 v61, v61, 0x3dd53b94, v138
	v_fmamk_f32 v62, v62, 0x3dd53b94, v138
	v_fmac_f32_e32 v165, 0x3dd53b94, v63
	v_exp_f32_e32 v222, v48
	v_exp_f32_e32 v224, v49
	v_exp_f32_e32 v220, v50
	v_exp_f32_e32 v223, v51
	v_exp_f32_e32 v219, v52
	v_exp_f32_e32 v221, v53
	v_exp_f32_e32 v217, v54
	v_exp_f32_e32 v218, v55
	v_exp_f32_e32 v212, v56
	v_exp_f32_e32 v214, v57
	v_exp_f32_e32 v211, v58
	v_exp_f32_e32 v213, v59
	v_exp_f32_e32 v208, v60
	v_exp_f32_e32 v210, v61
	v_exp_f32_e32 v207, v62
	v_exp_f32_e32 v209, v165
	s_waitcnt vmcnt(0)
	v_mov_b64_e32 v[46:47], v[14:15]
	v_mov_b64_e32 v[30:31], v[14:15]
	v_mov_b64_e32 v[62:63], v[14:15]
	s_mov_b32 s8, -1
	v_mov_b64_e32 v[44:45], v[12:13]
	v_mov_b64_e32 v[42:43], v[10:11]
	v_mov_b64_e32 v[40:41], v[8:9]
	v_mov_b64_e32 v[38:39], v[6:7]
	v_mov_b64_e32 v[36:37], v[4:5]
	v_mov_b64_e32 v[34:35], v[2:3]
	v_mov_b64_e32 v[32:33], v[0:1]
	v_mov_b64_e32 v[28:29], v[12:13]
	v_mov_b64_e32 v[26:27], v[10:11]
	v_mov_b64_e32 v[24:25], v[8:9]
	v_mov_b64_e32 v[22:23], v[6:7]
	v_mov_b64_e32 v[20:21], v[4:5]
	v_mov_b64_e32 v[18:19], v[2:3]
	v_mov_b64_e32 v[16:17], v[0:1]
	v_lshl_add_u32 v189, v188, 2, s12
	s_add_i32 s13, s60, 0x4080
	s_add_i32 s83, s60, 0x4040
	s_sub_i32 s14, s61, 64
	v_pk_fma_f32 v[134:135], v[78:79], s[26:27], v[138:139] op_sel_hi:[1,0,0]
	v_pk_fma_f32 v[160:161], v[76:77], s[26:27], v[138:139] op_sel_hi:[1,0,0]
	v_pk_fma_f32 v[162:163], v[74:75], s[26:27], v[138:139] op_sel_hi:[1,0,0]
	v_pk_fma_f32 v[128:129], v[72:73], s[26:27], v[138:139] op_sel_hi:[1,0,0]
	v_pk_fma_f32 v[130:131], v[70:71], s[26:27], v[138:139] op_sel_hi:[1,0,0]
	v_pk_fma_f32 v[132:133], v[68:69], s[26:27], v[138:139] op_sel_hi:[1,0,0]
	v_pk_fma_f32 v[136:137], v[66:67], s[26:27], v[138:139] op_sel_hi:[1,0,0]
	v_pk_fma_f32 v[138:139], v[64:65], s[26:27], v[138:139] op_sel_hi:[1,0,0]
	v_cndmask_b32_e64 v197, v164, 1.0, vcc
	v_mov_b64_e32 v[60:61], v[12:13]
	v_mov_b64_e32 v[58:59], v[10:11]
	v_mov_b64_e32 v[56:57], v[8:9]
	v_mov_b64_e32 v[54:55], v[6:7]
	v_mov_b64_e32 v[52:53], v[4:5]
	v_mov_b64_e32 v[50:51], v[2:3]
	v_mov_b64_e32 v[48:49], v[0:1]
	s_waitcnt vmcnt(4)
	ds_write_b128 v175, v[80:83] offset:16384
	s_waitcnt vmcnt(3)
	ds_write_b128 v176, v[84:87] offset:16384
	s_waitcnt vmcnt(2)
	ds_write_b128 v177, v[88:91] offset:49152
	s_waitcnt vmcnt(1)
	ds_write_b128 v178, v[92:95] offset:49152
	s_waitcnt vmcnt(0)
	ds_write_b128 v196, v[200:203]
	s_nop 0
	s_nop 0
	s_nop 0
	s_nop 0
	s_nop 0
	s_nop 0
	s_nop 0
	s_nop 0
	s_nop 0
	s_nop 0
	s_waitcnt lgkmcnt(0)
	s_barrier
